# P6: accumulators start from the x residual tile (waves 1-7 fetch it before the P5->P6 grid barrier, wave 0 at P6 start); epilogue only stores
# baseline (speedup 1.0000x reference)
; #define LAS __attribute__((address_space(3)))
;     __device__ __forceinline__ bool next(int i, Unit& u) const {
;         const long L = (long)i * G + c; if (L >= nwg) return false;
;         int wgid = (int)L; { const int q = nwg / NXCD, r = nwg % NXCD, xcd = wgid % NXCD, off = wgid / NXCD; wgid = (xcd < r ? xcd * (q + 1) : r * (q + 1) + (xcd - r) * q) + off; }
;         const int nig = WGM * nN, gid = wgid / nig, fm = gid * WGM, gsz = (nM - fm) < WGM ? (nM - fm) : WGM;
;         u.pm = fm + ((wgid % nig) % gsz); u.pn = (wgid % nig) / gsz; u.e = 0; u.nrows = BM; return true;
;     }
;     __device__ __forceinline__ void a_off(const Unit& u, const int (&R)[2], const int (&C)[2], unsigned (&off)[2][2]) const {
; #pragma unroll
;         for (int h = 0; h < 2; ++h)
; #pragma unroll
;             for (int i = 0; i < 2; ++i) off[h][i] = (unsigned)((u.pm * BM + h * HALF + R[i]) * RB + C[i] * 2);
;     }
;     __device__ __forceinline__ const char* b_base(const Unit& u) const { return (const char*)Bt + (size_t)u.pn * BM * RB; }
;     __device__ __forceinline__ void a_off_next(const Unit& u, const int (&R)[2], const int (&C)[2], unsigned (&off)[2][2], LAS unsigned char*) const { a_off(u, R, C, off); }
;     __device__ __forceinline__ void operator()(const f32x4 (&acc)[2][2][4][2], const Unit& u, int wr, int wc, int fr, int fq, const LAS float* bl) const {
;         const int row0 = u.pm * BM + wr * 64 + fr, col0 = u.pn * BM + wc * 32 + 8 * fq;
; #pragma unroll
;         for (int ai = 0; ai < 2; ++ai)
; #pragma unroll
;             for (int m = 0; m < 4; ++m) { bf16* rowp = O + (size_t)(row0 + ai * HALF + m * 16) * ldc + col0;
; #pragma unroll
;                 for (int bj = 0; bj < 2; ++bj) { const f32x4 v0 = acc[ai][bj][m][0], v1 = acc[ai][bj][m][1];
;                     u32x4 w; w.x = cvt_pk_bf16(v0[0], v0[1]); w.y = cvt_pk_bf16(v0[2], v0[3]); w.z = cvt_pk_bf16(v1[0], v1[1]); w.w = cvt_pk_bf16(v1[2], v1[3]);
;                     *(u32x4*)(rowp + bj * HALF) = w; } }
;     }
;     __device__ __forceinline__ void operator()(const f32x4 (&acc)[2][2][4][2], const Unit& u, int wr, int wc, int fr, int fq, const LAS float* bl) const {
;         const int row0 = u.pm * BM + wr * 64 + fr, col0 = u.pn * BM + wc * 32 + 4 * fq;
; #pragma unroll
;         for (int ai = 0; ai < 2; ++ai) {
;             f32x4 res[4][2][2];
; #pragma unroll
.LBB0_1024:
	v_readlane_b32 s0, v252, 0
	v_readlane_b32 s1, v252, 1
	s_cmp_lt_i32 s0, 6
	s_cselect_b64 s[6:7], -1, 0
	s_cmp_gt_i32 s1, 6
	s_cselect_b64 s[4:5], -1, 0
	s_and_b64 s[6:7], s[6:7], s[4:5]
	s_andn2_b64 vcc, exec, s[6:7]
	s_cbranch_vccnz .LBB0_1078
	s_waitcnt vmcnt(0)
	v_readlane_b32 s0, v252, 4
	v_readlane_b32 s1, v252, 5
	s_waitcnt vmcnt(0) lgkmcnt(0)
	s_barrier
	s_cmpk_gt_i32 s2, 0xff
	s_cbranch_scc1 .Lp6x_skip
	s_load_dwordx2 s[14:15], s[94:95], 0x0
	s_ashr_i32 s8, s2, 31
	s_lshr_b32 s8, s8, 29
	s_add_i32 s12, s2, s8
	s_and_b32 s8, s12, -8
	s_sub_i32 s10, s2, s8
	s_cmp_gt_i32 s10, -1
	s_cbranch_scc0 .Lp6x_neg
	s_lshl_b32 s11, s10, 5
	s_ashr_i32 s8, s12, 3
	s_branch .Lp6x_join
.Lp6x_neg:
	s_ashr_i32 s8, s12, 3
	s_mul_i32 s11, s10, 33
.Lp6x_join:
	s_add_i32 s8, s11, s8
	s_ashr_i32 s9, s8, 31
	s_lshr_b32 s9, s9, 27
	s_add_i32 s9, s8, s9
	s_ashr_i32 s10, s9, 5
	s_and_b32 s9, s9, 0xffe0
	s_sub_i32 s8, s8, s9
	s_bfe_i32 s9, s8, 0x80000
	s_bfe_u32 s9, s9, 0x2000d
	s_add_i32 s9, s8, s9
	s_bfe_i32 s11, s9, 0x80000
	s_and_b32 s9, s9, 0xfc
	s_sub_i32 s8, s8, s9
	s_lshl_b32 s10, s10, 2
	s_sext_i32_i16 s11, s11
	s_sext_i32_i8 s8, s8
	s_add_i32 s10, s10, s8
	s_ashr_i32 s11, s11, 2
	v_readfirstlane_b32 s16, v0
	v_and_b32_e32 v244, 15, v0
	v_bfe_u32 v245, v0, 4, 2
	s_ashr_i32 s17, s16, 8
	s_ashr_i32 s18, s16, 6
	s_lshl_b32 s18, s18, 5
	s_and_b32 s18, s18, 0x60
	v_lshl_or_b32 v244, s17, 6, v244
	v_lshl_or_b32 v245, v245, 2, s18
	v_lshl_add_u32 v244, s10, 8, v244
	v_lshl_or_b32 v245, s11, 8, v245
	v_lshlrev_b32_e32 v244, 13, v244
	v_lshl_add_u32 v244, v245, 2, v244
	v_add_u32_e32 v245, 0x20000, v244
	v_add_u32_e32 v246, 0x40000, v244
	v_add_u32_e32 v247, 0x60000, v244
	v_add_u32_e32 v248, 0x100000, v244
	v_add_u32_e32 v249, 0x120000, v244
	v_add_u32_e32 v250, 0x140000, v244
	v_add_u32_e32 v251, 0x160000, v244
	s_waitcnt lgkmcnt(0)
	s_cmp_lt_u32 s16, 64
	s_cbranch_scc1 .Lp6x_skip
	global_load_dwordx4 v[126:129], v244, s[14:15] nt
	global_load_dwordx4 v[122:125], v244, s[14:15] offset:64 nt
	global_load_dwordx4 v[114:117], v244, s[14:15] offset:512 nt
	global_load_dwordx4 v[106:109], v244, s[14:15] offset:576 nt
	global_load_dwordx4 v[118:121], v245, s[14:15] nt
	global_load_dwordx4 v[110:113], v245, s[14:15] offset:64 nt
	global_load_dwordx4 v[98:101], v245, s[14:15] offset:512 nt
	global_load_dwordx4 v[90:93], v245, s[14:15] offset:576 nt
	global_load_dwordx4 v[102:105], v246, s[14:15] nt
	global_load_dwordx4 v[94:97], v246, s[14:15] offset:64 nt
	global_load_dwordx4 v[82:85], v246, s[14:15] offset:512 nt
	global_load_dwordx4 v[78:81], v246, s[14:15] offset:576 nt
	global_load_dwordx4 v[86:89], v247, s[14:15] nt
	global_load_dwordx4 v[74:77], v247, s[14:15] offset:64 nt
	global_load_dwordx4 v[70:73], v247, s[14:15] offset:512 nt
	global_load_dwordx4 v[66:69], v247, s[14:15] offset:576 nt
	global_load_dwordx4 v[54:57], v248, s[14:15] nt
	global_load_dwordx4 v[50:53], v248, s[14:15] offset:64 nt
	global_load_dwordx4 v[42:45], v248, s[14:15] offset:512 nt
	global_load_dwordx4 v[34:37], v248, s[14:15] offset:576 nt
	global_load_dwordx4 v[46:49], v249, s[14:15] nt
	global_load_dwordx4 v[38:41], v249, s[14:15] offset:64 nt
	global_load_dwordx4 v[26:29], v249, s[14:15] offset:512 nt
	global_load_dwordx4 v[10:13], v249, s[14:15] offset:576 nt
	global_load_dwordx4 v[30:33], v250, s[14:15] nt
	global_load_dwordx4 v[18:21], v250, s[14:15] offset:64 nt
	global_load_dwordx4 v[62:65], v250, s[14:15] offset:512 nt
	global_load_dwordx4 v[58:61], v250, s[14:15] offset:576 nt
	global_load_dwordx4 v[14:17], v251, s[14:15] nt
	global_load_dwordx4 v[6:9], v251, s[14:15] offset:64 nt
	global_load_dwordx4 v[22:25], v251, s[14:15] offset:512 nt
	global_load_dwordx4 v[2:5], v251, s[14:15] offset:576 nt
.Lp6x_skip:
	s_and_saveexec_b64 s[6:7], s[0:1]
	s_cbranch_execz .LBB0_1077
	s_add_i32 s8, 0, 0x23820
	v_mov_b32_e32 v1, s8
	s_waitcnt vmcnt(0) expcnt(0) lgkmcnt(0)
	ds_read_b32 v3, v1
	s_add_i32 s8, 0, 0x23824
	v_mov_b32_e32 v1, s8
	ds_read_b32 v1, v1
	s_waitcnt lgkmcnt(1)
	v_cmp_ne_u32_e32 vcc, 0, v3
	s_cbranch_vccnz .LBB0_1041
	s_add_u32 s8, s22, 0x4200
	s_addc_u32 s9, s23, 0
	s_add_u32 s10, s22, 0x4400
	s_addc_u32 s11, s23, 0
	s_add_u32 s12, s22, 0x4500
	s_addc_u32 s13, s23, 0
	s_add_u32 s14, s22, 0x4600
	s_addc_u32 s15, s23, 0
	s_add_u32 s16, s22, 0x4700
	s_addc_u32 s17, s23, 0
	s_add_u32 s28, s22, 0x4800
	s_addc_u32 s29, s23, 0
	s_add_u32 s30, s22, 0x4900
	s_addc_u32 s31, s23, 0
	s_add_u32 s34, s22, 0x4a00
	s_addc_u32 s35, s23, 0
	s_add_u32 s36, s22, 0x4b00
	s_addc_u32 s37, s23, 0
	s_add_u32 s38, s22, 0x4c00
	s_addc_u32 s39, s23, 0
	s_add_u32 s40, s22, 0x4d00
	s_addc_u32 s41, s23, 0
	s_add_u32 s42, s22, 0x4e00
	s_addc_u32 s43, s23, 0
	s_add_u32 s44, s22, 0x4f00
	s_addc_u32 s45, s23, 0
	s_add_u32 s46, s22, 0x5000
	s_addc_u32 s47, s23, 0
	s_add_u32 s48, s22, 0x5100
	s_addc_u32 s49, s23, 0
	s_add_u32 s50, s22, 0x5200
	s_addc_u32 s51, s23, 0
	s_add_u32 s52, s22, 0x5300
	s_addc_u32 s53, s23, 0
	s_mov_b32 s18, 1
	v_mov_b32_e32 v17, 0
	s_branch .LBB0_1029

; template <class Epi, class Sched, bool ALIGN_EPI, bool FP8 = false>
; __device__ __forceinline__ void gemm_phase(LAS unsigned char* lds, const Gemm g, const Sched& S, const Epi& E) {
;     ...
;     const int tid = tid_, wid = __builtin_amdgcn_readfirstlane(tid >> 6), lane = tid & 63, wr = wid >> 2, wc = wid & 3, fr = lane & 15, fq = lane >> 4;
;     const int RB = g.RB, nt = RB / (BK * 2);
;     int sR[2], sC[2]; unsigned voffB[2];
; #pragma unroll
;     for (int i = 0; i < 2; ++i) { stage_rc(tid * 16 + i * 8192, sR[i], sC[i]); const int Rb = Epi::PERM ? ((sR[i] & ~31) + perm32(sR[i] & 31)) : sR[i]; voffB[i] = (unsigned)(Rb * RB + sC[i] * 2); }
;     const size_t kstep = (size_t)(BK * 2);
;     const size_t hstep = (size_t)HALF * RB;
;     const unsigned ldsw = (unsigned)wid * 1024u;
;     const int aoff = lds_byte(wr * 64 + fr, fq * 8), boff = lds_byte(wc * 32 + fr, fq * 8);
;     __device__ __forceinline__ void operator()(const f32x4 (&acc)[2][2][4][2], const Unit& u, int wr, int wc, int fr, int fq, const LAS float* bl) const {
;     ...
;             for (int m = 0; m < 4; ++m) { const size_t off = (size_t)(row0 + ai * HALF + m * 16) * ldc + col0;
; #pragma unroll
;                 for (int bj = 0; bj < 2; ++bj)
; #pragma unroll
;                     for (int n = 0; n < 2; ++n) res[m][bj][n] = __builtin_nontemporal_load((const f32x4*)(base + off + bj * HALF + n * 16)); }
.LBB0_1085:
	s_load_dwordx2 s[12:13], s[6:7], 0x0
	s_andn2_b64 vcc, exec, s[8:9]
	s_cbranch_vccnz .LBB0_1115
	v_readlane_b32 s98, v252, 0
	s_cmp_lt_i32 s98, 6
	s_cselect_b32 s98, 1, 0
	v_bfe_i32 v234, v1, 27, 1
	v_lshlrev_b32_e32 v232, 4, v1
	v_lshrrev_b32_e32 v234, 22, v234
	v_add_u32_e32 v234, v232, v234
	v_and_b32_e32 v234, 0xfffffc00, v234
	v_sub_u32_e32 v234, v232, v234
	v_lshrrev_b32_e32 v235, 4, v234
	v_bitop3_b32 v234, v235, v234, 32 bitop3:0x6c
	v_ashrrev_i32_e32 v236, 31, v234
	v_ashrrev_i32_e32 v233, 31, v1
	v_lshrrev_b32_e32 v236, 26, v236
	v_lshrrev_b32_e32 v233, 26, v233
	v_add_u32_e32 v236, v234, v236
	v_add_u32_e32 v233, v1, v233
	v_ashrrev_i32_e32 v237, 6, v236
	v_and_b32_e32 v236, 0xc0, v236
	v_ashrrev_i32_e32 v233, 6, v233
	v_sub_u32_e32 v234, v234, v236
	v_mov_b32_e32 v210, 1
	v_lshlrev_b32_e32 v235, 3, v233
	v_lshlrev_b32_e32 v233, 5, v233
	v_ashrrev_i16_sdwa v234, v210, sext(v234) dst_sel:DWORD dst_unused:UNUSED_PAD src0_sel:DWORD src1_sel:BYTE_0
	v_and_b32_e32 v233, 32, v233
	v_bfe_i32 v234, v234, 0, 16
	v_add_u32_e32 v232, 0x2000, v232
	v_add_lshl_u32 v233, v233, v234, 1
	v_ashrrev_i32_e32 v234, 31, v232
	v_lshrrev_b32_e32 v234, 22, v234
	v_add_u32_e32 v234, v232, v234
	v_ashrrev_i32_e32 v234, 10, v234
	v_mul_i32_i24_e32 v236, 0x400, v234
	v_sub_u32_e32 v232, v232, v236
	v_lshrrev_b32_e32 v236, 4, v232
	v_and_b32_e32 v235, -16, v235
	v_bitop3_b32 v232, v236, v232, 32 bitop3:0x6c
	v_add_u32_e32 v235, v237, v235
	v_ashrrev_i32_e32 v237, 31, v232
	v_lshrrev_b32_e32 v237, 26, v237
	v_add_u32_e32 v237, v232, v237
	s_waitcnt lgkmcnt(0)
	s_cmp_lt_u32 s40, 64
	s_cbranch_scc0 .Lp6x_w0done
	s_cmp_eq_u32 s98, 1
	s_cbranch_scc0 .Lp6x_w0done
	global_load_dwordx4 v[126:129], v244, s[12:13] nt
	global_load_dwordx4 v[122:125], v244, s[12:13] offset:64 nt
	global_load_dwordx4 v[114:117], v244, s[12:13] offset:512 nt
	global_load_dwordx4 v[106:109], v244, s[12:13] offset:576 nt
	global_load_dwordx4 v[118:121], v245, s[12:13] nt
	global_load_dwordx4 v[110:113], v245, s[12:13] offset:64 nt
	global_load_dwordx4 v[98:101], v245, s[12:13] offset:512 nt
	global_load_dwordx4 v[90:93], v245, s[12:13] offset:576 nt
	global_load_dwordx4 v[102:105], v246, s[12:13] nt
	global_load_dwordx4 v[94:97], v246, s[12:13] offset:64 nt
	global_load_dwordx4 v[82:85], v246, s[12:13] offset:512 nt
	global_load_dwordx4 v[78:81], v246, s[12:13] offset:576 nt
	global_load_dwordx4 v[86:89], v247, s[12:13] nt
	global_load_dwordx4 v[74:77], v247, s[12:13] offset:64 nt
	global_load_dwordx4 v[70:73], v247, s[12:13] offset:512 nt
	global_load_dwordx4 v[66:69], v247, s[12:13] offset:576 nt
	global_load_dwordx4 v[54:57], v248, s[12:13] nt
	global_load_dwordx4 v[50:53], v248, s[12:13] offset:64 nt
	global_load_dwordx4 v[42:45], v248, s[12:13] offset:512 nt
	global_load_dwordx4 v[34:37], v248, s[12:13] offset:576 nt
	global_load_dwordx4 v[46:49], v249, s[12:13] nt
	global_load_dwordx4 v[38:41], v249, s[12:13] offset:64 nt
	global_load_dwordx4 v[26:29], v249, s[12:13] offset:512 nt
	global_load_dwordx4 v[10:13], v249, s[12:13] offset:576 nt
	global_load_dwordx4 v[30:33], v250, s[12:13] nt
	global_load_dwordx4 v[18:21], v250, s[12:13] offset:64 nt
	global_load_dwordx4 v[62:65], v250, s[12:13] offset:512 nt
	global_load_dwordx4 v[58:61], v250, s[12:13] offset:576 nt
	global_load_dwordx4 v[14:17], v251, s[12:13] nt
	global_load_dwordx4 v[6:9], v251, s[12:13] offset:64 nt
	global_load_dwordx4 v[22:25], v251, s[12:13] offset:512 nt
	global_load_dwordx4 v[2:5], v251, s[12:13] offset:576 nt
; #define PG8_STAGE(bufoff, gbase, voff) do { _Pragma("unroll") for (int _i = 0; _i < 2; ++_i) \
;         __builtin_amdgcn_global_load_lds((const unsigned*)((const char*)(gbase) + (voff)[_i]), (LAS unsigned*)(lds + (bufoff) + ldsw + _i * 8192), 16, 0, 0); } while (0)
; #define PG8_WAIT_V(n) asm volatile("s_waitcnt vmcnt(" #n ")" ::: "memory")
; #define PG8_BAR __builtin_amdgcn_s_barrier()
;     __device__ __forceinline__ const char* b_base(const Unit& u) const { return (const char*)Bt + (size_t)u.pn * BM * RB; }
;     __device__ __forceinline__ void a_off(const Unit& u, const int (&R)[2], const int (&C)[2], unsigned (&off)[2][2]) const { wait_tile(u.pm); a_off_plain(u, R, C, off); }
; template <class Epi, class Sched, bool ALIGN_EPI, bool FP8 = false>
; __device__ __forceinline__ void gemm_phase(LAS unsigned char* lds, const Gemm g, const Sched& S, const Epi& E) {
;     ...
; #pragma unroll
;     for (int i = 0; i < 2; ++i) { stage_rc(tid * 16 + i * 8192, sR[i], sC[i]); const int Rb = Epi::PERM ? ((sR[i] & ~31) + perm32(sR[i] & 31)) : sR[i]; voffB[i] = (unsigned)(Rb * RB + sC[i] * 2); }
;     const size_t kstep = (size_t)(BK * 2);
;     const size_t hstep = (size_t)HALF * RB;
;     const unsigned ldsw = (unsigned)wid * 1024u;
;     const int aoff = lds_byte(wr * 64 + fr, fq * 8), boff = lds_byte(wc * 32 + fr, fq * 8);
;     const char* Ab = (const char*)g.A;
;     ...
;     Unit cur, nxt; int ui = 0, prev_pm = 0;
;     if (!S.next(0, cur)) return;
;     f32x4 acc[2][2][4][2];
; #pragma unroll
;     for (int a = 0; a < 2; ++a)
; #pragma unroll
;         for (int b = 0; b < 2; ++b)
; #pragma unroll
;             for (int m = 0; m < 4; ++m)
; #pragma unroll
;                 for (int n = 0; n < 2; ++n) acc[a][b][m][n] = (f32x4){0.f, 0.f, 0.f, 0.f};
;     typename FragT<FP8>::T At[4], B0[2], B1[2];
;     unsigned ao[2][2];
;     S.a_off(cur, sR, sC, ao);
;     const char* cB = S.b_base(cur);
;     PG8_STAGE(PG8_SB(0, 0), cB, voffB); PG8_STAGE(PG8_SB(0, 1), cB + hstep, voffB); PG8_STAGE(PG8_SA(0, 0), Ab, ao[0]); PG8_STAGE(PG8_SA(0, 1), Ab, ao[1]);
;     if (wr == 1) PG8_BAR;
;     PG8_WAIT_V(2); PG8_BAR;
;     PG8_STAGE(PG8_SB(1, 0), cB + kstep, voffB); PG8_STAGE(PG8_SA(1, 0), Ab + kstep, ao[0]); PG8_STAGE(PG8_SB(1, 1), cB + hstep + kstep, voffB);
;     PG8_WAIT_V(6); PG8_BAR;
.Lp6x_w0done:
	s_add_u32 s18, s4, 0x1600000
	v_ashrrev_i32_e32 v238, 6, v237
	v_and_b32_e32 v237, 0xc0, v237
	s_addc_u32 s19, s5, 0
	v_sub_u32_e32 v232, v232, v237
	s_add_u32 s14, s4, 0x38200000
	v_lshlrev_b32_e32 v236, 3, v234
	v_lshlrev_b32_e32 v234, 5, v234
	v_ashrrev_i16_sdwa v232, v210, sext(v232) dst_sel:DWORD dst_unused:UNUSED_PAD src0_sel:DWORD src1_sel:BYTE_0
	s_addc_u32 s15, s5, 0
	v_and_b32_e32 v236, -16, v236
	v_and_b32_e32 v234, 32, v234
	v_bfe_i32 v232, v232, 0, 16
	s_lshl_b32 s6, s75, 8
	v_add_u32_e32 v236, v238, v236
	v_add_lshl_u32 v232, v234, v232, 1
	v_add_u32_e32 v234, s6, v235
	v_lshl_add_u32 v198, v234, 12, v233
	v_add_u32_e32 v234, s6, v236
	s_bitset1_b32 s6, 7
	s_ashr_i32 s9, s40, 6
	v_lshl_add_u32 v200, v234, 12, v232
	v_add_u32_e32 v234, s6, v235
	s_ashr_i32 s55, s54, 31
	s_ashr_i32 s8, s40, 8
	v_lshl_add_u32 v194, v235, 12, v233
	s_lshl_b32 s16, s9, 10
	v_lshl_add_u32 v211, v234, 12, v233
	v_add_u32_e32 v233, s6, v236
	s_lshl_b64 s[6:7], s[54:55], 20
	s_add_u32 s6, s18, s6
	s_addc_u32 s7, s19, s7
	s_add_i32 s24, s16, 0
	s_add_i32 s25, s24, 0x10000
	s_add_i32 s26, s24, 0x12000
	s_mov_b32 m0, s25
	s_add_u32 s16, s6, 0x80000
	v_lshl_add_u32 v196, v236, 12, v232
	global_load_lds_dwordx4 v194, s[6:7]
	s_mov_b32 m0, s26
	s_addc_u32 s17, s7, 0
	s_add_i32 s27, s24, 0x14000
	global_load_lds_dwordx4 v196, s[6:7]
	s_mov_b32 m0, s27
	s_add_i32 s55, s24, 0x16000
	global_load_lds_dwordx4 v194, s[16:17]
	s_mov_b32 m0, s55
	s_add_i32 s62, s24, 0x2000
	global_load_lds_dwordx4 v196, s[16:17]
	s_mov_b32 m0, s24
	s_add_i32 s63, s24, 0x4000
	global_load_lds_dwordx4 v198, s[14:15]
	s_mov_b32 m0, s62
	s_add_i32 s64, s24, 0x6000
	global_load_lds_dwordx4 v200, s[14:15]
	s_mov_b32 m0, s63
	v_lshl_add_u32 v212, v233, 12, v232
	global_load_lds_dwordx4 v211, s[14:15]
	s_mov_b32 m0, s64
	v_mov_b32_e32 v199, 0
	global_load_lds_dwordx4 v212, s[14:15]
	v_mov_b32_e32 v195, v199
	v_mov_b32_e32 v197, v199
	s_cmp_eq_u32 s8, 1
	s_mov_b32 s65, 0
	v_lshl_add_u64 v[234:235], s[6:7], 0, v[194:195]
	v_lshl_add_u64 v[232:233], s[6:7], 0, v[196:197]
	s_cselect_b64 s[16:17], -1, 0
	s_cmp_lg_u32 s8, 1
	v_mov_b32_e32 v201, v199
	s_cbranch_scc1 .LBB0_1088
	s_barrier
.LBB0_1088:
	s_add_u32 s28, s4, 0x41e00000
	s_addc_u32 s29, s5, 0
	s_lshl_b32 s9, s9, 5
	s_and_b32 s9, s9, 0x60
	s_lshl_b32 s20, s8, 13
	s_lshl_b32 s21, s9, 7
	s_add_i32 s66, s24, 0x18000
	s_mov_b64 s[30:31], 0x80
	s_add_i32 s67, s24, 0x1a000
	v_lshl_add_u64 v[234:235], v[234:235], 0, s[30:31]
	s_mov_b32 m0, s66
	s_add_u32 s34, s4, 0x38200080
	s_waitcnt vmcnt(2)
	s_barrier
	global_load_lds_dwordx4 v[234:235], off
	v_lshl_add_u64 v[232:233], v[232:233], 0, s[30:31]
	s_mov_b32 m0, s67
	s_addc_u32 s35, s5, 0
	s_add_i32 s68, s24, 0x8000
	s_add_i32 s69, s24, 0xa000
	global_load_lds_dwordx4 v[232:233], off
	v_lshl_add_u64 v[232:233], s[34:35], 0, v[198:199]
	s_mov_b32 m0, s68
	s_add_u32 s4, s6, 0x80080
	global_load_lds_dwordx4 v[232:233], off
	v_lshl_add_u64 v[232:233], s[34:35], 0, v[200:201]
	s_mov_b32 m0, s69
	s_addc_u32 s5, s7, 0
	s_add_i32 s70, s24, 0x1c000
	global_load_lds_dwordx4 v[232:233], off
	v_lshl_add_u64 v[232:233], s[4:5], 0, v[194:195]
	s_mov_b32 m0, s70
	s_add_i32 s71, s24, 0x1e000
	global_load_lds_dwordx4 v[232:233], off
	v_lshl_add_u64 v[232:233], s[4:5], 0, v[196:197]
	s_mov_b32 m0, s71
	s_cmp_lt_i32 s8, 4
	global_load_lds_dwordx4 v[232:233], off
	v_bfe_u32 v233, v1, 4, 2
	v_and_b32_e32 v232, 15, v1
	v_lshlrev_b32_e32 v234, 4, v233
	v_lshl_or_b32 v213, s8, 6, v232
	v_lshl_or_b32 v232, v232, 6, v234
	v_lshlrev_b32_e32 v234, 2, v1
	v_and_b32_e32 v234, 32, v234
	v_bitop3_b32 v235, v232, s20, v234 bitop3:0xde
	v_bitop3_b32 v232, v232, s21, v234 bitop3:0xde
	s_waitcnt vmcnt(6)
	s_cselect_b64 s[36:37], -1, 0
	s_cmp_lt_i32 s8, 2
	s_cselect_b64 s[38:39], -1, 0
	s_cmpk_lt_u32 s40, 0x100
	v_add_u32_e32 v215, 0, v232
	s_cselect_b64 s[40:41], -1, 0
	s_ashr_i32 s72, s3, 31
	s_ashr_i32 s73, s2, 31
	v_lshl_or_b32 v214, v233, 2, s9
	v_mov_b64_e32 v[202:203], 0x100
	v_mov_b64_e32 v[204:205], 0xff
	v_add_u32_e32 v216, 0x10000, v215
	v_add_u32_e32 v217, 0x14000, v215
	v_add_u32_e32 v218, 0, v235
	v_cndmask_b32_e64 v219, 0, 1, s[36:37]
	s_mov_b64 s[42:43], 0x100000
	s_mov_b64 s[44:45], 0x120000
	s_mov_b64 s[46:47], 0x140000
	s_mov_b64 s[48:49], 0x160000
	s_barrier
	s_branch .LBB0_1091

; #define PG8_STAGE(bufoff, gbase, voff) do { _Pragma("unroll") for (int _i = 0; _i < 2; ++_i) \
;         __builtin_amdgcn_global_load_lds((const unsigned*)((const char*)(gbase) + (voff)[_i]), (LAS unsigned*)(lds + (bufoff) + ldsw + _i * 8192), 16, 0, 0); } while (0)
; #define PG8_WAIT_V(n) asm volatile("s_waitcnt vmcnt(" #n ")" ::: "memory")
; #define PG8_BAR __builtin_amdgcn_s_barrier()
;     __device__ __forceinline__ const char* b_base(const Unit& u) const { return (const char*)Bt + (size_t)u.pn * BM * RB; }
; template <class Epi, class Sched, bool ALIGN_EPI, bool FP8 = false>
; __device__ __forceinline__ void gemm_phase(LAS unsigned char* lds, const Gemm g, const Sched& S, const Epi& E) {
;     ...
;     Unit cur, nxt; int ui = 0, prev_pm = 0;
;     if (!S.next(0, cur)) return;
;     f32x4 acc[2][2][4][2];
; #pragma unroll
;     for (int a = 0; a < 2; ++a)
; #pragma unroll
;         for (int b = 0; b < 2; ++b)
; #pragma unroll
;             for (int m = 0; m < 4; ++m)
; #pragma unroll
;                 for (int n = 0; n < 2; ++n) acc[a][b][m][n] = (f32x4){0.f, 0.f, 0.f, 0.f};
;     typename FragT<FP8>::T At[4], B0[2], B1[2];
;     unsigned ao[2][2];
;     S.a_off(cur, sR, sC, ao);
;     const char* cB = S.b_base(cur);
;     PG8_STAGE(PG8_SB(0, 0), cB, voffB); PG8_STAGE(PG8_SB(0, 1), cB + hstep, voffB); PG8_STAGE(PG8_SA(0, 0), Ab, ao[0]); PG8_STAGE(PG8_SA(0, 1), Ab, ao[1]);
;     if (wr == 1) PG8_BAR;
;     PG8_WAIT_V(2); PG8_BAR;
;     PG8_STAGE(PG8_SB(1, 0), cB + kstep, voffB); PG8_STAGE(PG8_SA(1, 0), Ab + kstep, ao[0]); PG8_STAGE(PG8_SB(1, 1), cB + hstep + kstep, voffB);
;     PG8_WAIT_V(6); PG8_BAR;
;     for (;;) {
;         const bool has_next = S.next(ui + 1, nxt);
;         S.prefetch(lds + AUX_OFF, cur, has_next, nxt, ui, wid, lane);
;         const char* nB = has_next ? S.b_base(nxt) : cB;
;     __device__ __forceinline__ bool next(int i, Unit& u) const {
;         const long L = (long)i * G + c; if (L >= nwg) return false;
;         int wgid = (int)L; { const int q = nwg / NXCD, r = nwg % NXCD, xcd = wgid % NXCD, off = wgid / NXCD; wgid = (xcd < r ? xcd * (q + 1) : r * (q + 1) + (xcd - r) * q) + off; }
;         const int nig = WGM * nN, gid = wgid / nig, fm = gid * WGM, gsz = (nM - fm) < WGM ? (nM - fm) : WGM;
;         u.pm = fm + ((wgid % nig) % gsz); u.pn = (wgid % nig) / gsz; u.e = 0; u.nrows = BM; return true;
.LBB0_1096:
	s_ashr_i32 s8, s20, 3
	s_add_i32 s8, s50, s8
	s_ashr_i32 s9, s8, 31
	s_lshr_b32 s9, s9, 27
	s_add_i32 s9, s8, s9
	s_ashr_i32 s20, s9, 5
	s_lshl_b32 s20, s20, 2
	s_sub_i32 s21, 32, s20
	s_min_i32 s21, s21, 4
	s_abs_i32 s50, s21
	v_cvt_f32_u32_e32 v232, s50
	s_sub_i32 s52, 0, s50
	s_andn2_b32 s9, s9, 31
	s_sub_i32 s8, s8, s9
	v_rcp_iflag_f32_e32 v232, v232
	s_abs_i32 s9, s8
	s_xor_b32 s51, s8, s21
	s_ashr_i32 s51, s51, 31
	v_mul_f32_e32 v232, 0x4f7ffffe, v232
	v_cvt_u32_f32_e32 v232, v232
	s_nop 0
	v_readfirstlane_b32 s53, v232
	s_mul_i32 s52, s52, s53
	s_mul_hi_u32 s52, s53, s52
	s_add_i32 s53, s53, s52
	s_mul_hi_u32 s52, s9, s53
	s_mul_i32 s53, s52, s50
	s_sub_i32 s9, s9, s53
	s_add_i32 s56, s52, 1
	s_sub_i32 s53, s9, s50
	s_cmp_ge_u32 s9, s50
	s_cselect_b32 s52, s56, s52
	s_cselect_b32 s9, s53, s9
	s_add_i32 s53, s52, 1
	s_cmp_ge_u32 s9, s50
	s_cselect_b32 s9, s53, s52
	s_xor_b32 s9, s9, s51
	s_sub_i32 s50, s9, s51
	s_mul_i32 s9, s50, s21
	s_sub_i32 s8, s8, s9
	s_add_i32 s74, s20, s8
.LBB0_1097:
	s_ashr_i32 s51, s50, 31
	s_lshl_b64 s[8:9], s[50:51], 20
	s_add_u32 s52, s18, s8
	s_addc_u32 s53, s19, s9
	s_and_b64 s[8:9], s[4:5], exec
	s_cselect_b32 s51, s53, s7
	s_cselect_b32 s76, s52, s6
	s_lshl_b32 s77, s74, 8
	s_or_b32 s78, s77, 0x80
	s_add_u32 s79, s6, 0x100
	s_addc_u32 s80, s7, 0
	s_mov_b32 s81, -2
	s_mov_b64 s[56:57], s[34:35]
	s_cmp_eq_u32 s65, s98
	s_cbranch_scc1 .LBB0_1099
	v_mov_b32_e32 v10, v199
	v_mov_b32_e32 v11, v199
	v_mov_b32_e32 v12, v199
	v_mov_b32_e32 v13, v199
	v_mov_b64_e32 v[28:29], v[12:13]
	v_mov_b64_e32 v[36:37], v[12:13]
	v_mov_b64_e32 v[44:45], v[12:13]
	v_mov_b64_e32 v[6:7], v[10:11]
	v_mov_b64_e32 v[16:17], v[12:13]
	v_mov_b64_e32 v[20:21], v[12:13]
	v_mov_b64_e32 v[32:33], v[12:13]
	v_mov_b64_e32 v[40:41], v[12:13]
	v_mov_b64_e32 v[48:49], v[12:13]
	v_mov_b64_e32 v[52:53], v[12:13]
	v_mov_b64_e32 v[56:57], v[12:13]
	v_mov_b64_e32 v[68:69], v[12:13]
	v_mov_b64_e32 v[72:73], v[12:13]
	v_mov_b64_e32 v[80:81], v[12:13]
	v_mov_b64_e32 v[84:85], v[12:13]
	v_mov_b64_e32 v[92:93], v[12:13]
	v_mov_b64_e32 v[100:101], v[12:13]
	v_mov_b64_e32 v[108:109], v[12:13]
	v_mov_b64_e32 v[116:117], v[12:13]
	v_mov_b64_e32 v[76:77], v[12:13]
	v_mov_b64_e32 v[88:89], v[12:13]
	v_mov_b64_e32 v[96:97], v[12:13]
	v_mov_b64_e32 v[104:105], v[12:13]
	v_mov_b64_e32 v[112:113], v[12:13]
	v_mov_b64_e32 v[120:121], v[12:13]
	v_mov_b64_e32 v[124:125], v[12:13]
	v_mov_b64_e32 v[128:129], v[12:13]
	v_mov_b64_e32 v[64:65], v[12:13]
	v_mov_b64_e32 v[60:61], v[12:13]
	v_mov_b64_e32 v[24:25], v[12:13]
	v_mov_b64_e32 v[2:3], v[10:11]
	v_mov_b64_e32 v[26:27], v[10:11]
	v_mov_b64_e32 v[34:35], v[10:11]
	v_mov_b64_e32 v[42:43], v[10:11]
	v_mov_b64_e32 v[8:9], v[12:13]
	v_mov_b64_e32 v[14:15], v[10:11]
	v_mov_b64_e32 v[18:19], v[10:11]
	v_mov_b64_e32 v[30:31], v[10:11]
	v_mov_b64_e32 v[38:39], v[10:11]
	v_mov_b64_e32 v[46:47], v[10:11]
	v_mov_b64_e32 v[50:51], v[10:11]
	v_mov_b64_e32 v[54:55], v[10:11]
	v_mov_b64_e32 v[66:67], v[10:11]
	v_mov_b64_e32 v[70:71], v[10:11]
	v_mov_b64_e32 v[78:79], v[10:11]
	v_mov_b64_e32 v[82:83], v[10:11]
	v_mov_b64_e32 v[90:91], v[10:11]
	v_mov_b64_e32 v[98:99], v[10:11]
	v_mov_b64_e32 v[106:107], v[10:11]
	v_mov_b64_e32 v[114:115], v[10:11]
	v_mov_b64_e32 v[74:75], v[10:11]
	v_mov_b64_e32 v[86:87], v[10:11]
	v_mov_b64_e32 v[94:95], v[10:11]
	v_mov_b64_e32 v[102:103], v[10:11]
	v_mov_b64_e32 v[110:111], v[10:11]
	v_mov_b64_e32 v[118:119], v[10:11]
	v_mov_b64_e32 v[122:123], v[10:11]
	v_mov_b64_e32 v[126:127], v[10:11]
	v_mov_b64_e32 v[62:63], v[10:11]
	v_mov_b64_e32 v[58:59], v[10:11]
	v_mov_b64_e32 v[22:23], v[10:11]
	v_mov_b64_e32 v[4:5], v[12:13]
	s_branch .LBB0_1099

; #define LAS __attribute__((address_space(3)))
;     __device__ void operator()(int r, int n, float v) const { if (r < NMETA) proj[(size_t)(M + r) * DINP + n] = f2bf(v); }
;     __device__ __forceinline__ void operator()(const f32x4 (&acc)[2][2][4][2], const Unit& u, int wr, int wc, int fr, int fq, const LAS float* bl) const {
;         const int row0 = u.pm * BM + wr * 64 + fr, col0 = u.pn * BM + wc * 32 + 4 * fq;
; #pragma unroll
;         for (int ai = 0; ai < 2; ++ai) {
;             f32x4 res[4][2][2];
; #pragma unroll
;             for (int m = 0; m < 4; ++m) { const size_t off = (size_t)(row0 + ai * HALF + m * 16) * ldc + col0;
; #pragma unroll
;                 for (int bj = 0; bj < 2; ++bj)
; #pragma unroll
;                     for (int n = 0; n < 2; ++n) res[m][bj][n] = __builtin_nontemporal_load((const f32x4*)(base + off + bj * HALF + n * 16)); }
; #pragma unroll
;             for (int m = 0; m < 4; ++m) { const size_t off = (size_t)(row0 + ai * HALF + m * 16) * ldc + col0;
; #pragma unroll
;                 for (int bj = 0; bj < 2; ++bj)
; #pragma unroll
;                     for (int n = 0; n < 2; ++n) *(f32x4*)(out + off + bj * HALF + n * 16) = res[m][bj][n] + acc[ai][bj][m][n]; }
;         }
.LBB0_1111:
	s_cmp_eq_u32 s65, s98
	s_cbranch_scc1 .Lp6x_epi
	s_waitcnt lgkmcnt(0)
	v_lshl_add_u32 v184, s75, 8, v213
	v_lshl_or_b32 v130, s54, 8, v214
	v_ashrrev_i32_e32 v185, 31, v184
	v_ashrrev_i32_e32 v131, 31, v130
	v_lshlrev_b64 v[134:135], 13, v[184:185]
	v_or_b32_e32 v152, 16, v184
	v_or_b32_e32 v168, 32, v184
	v_or_b32_e32 v184, 48, v184
	v_lshlrev_b64 v[130:131], 2, v[130:131]
	v_ashrrev_i32_e32 v153, 31, v152
	v_ashrrev_i32_e32 v169, 31, v168
	v_ashrrev_i32_e32 v185, 31, v184
	v_lshl_add_u64 v[132:133], s[12:13], 0, v[130:131]
	v_lshlrev_b64 v[192:193], 13, v[152:153]
	v_lshlrev_b64 v[224:225], 13, v[168:169]
	v_lshlrev_b64 v[226:227], 13, v[184:185]
	v_lshl_add_u64 v[148:149], v[132:133], 0, v[134:135]
	v_lshl_add_u64 v[164:165], v[132:133], 0, v[192:193]
	v_lshl_add_u64 v[180:181], v[132:133], 0, v[224:225]
	v_lshl_add_u64 v[220:221], v[132:133], 0, v[226:227]
	global_load_dwordx4 v[136:139], v[148:149], off nt
	global_load_dwordx4 v[140:143], v[148:149], off offset:64 nt
	global_load_dwordx4 v[144:147], v[148:149], off offset:512 nt
	s_nop 0
	global_load_dwordx4 v[148:151], v[148:149], off offset:576 nt
	s_nop 0
	global_load_dwordx4 v[152:155], v[164:165], off nt
	global_load_dwordx4 v[156:159], v[164:165], off offset:64 nt
	global_load_dwordx4 v[160:163], v[164:165], off offset:512 nt
	s_nop 0
	global_load_dwordx4 v[164:167], v[164:165], off offset:576 nt
	s_nop 0
	global_load_dwordx4 v[168:171], v[180:181], off nt
	global_load_dwordx4 v[172:175], v[180:181], off offset:64 nt
	global_load_dwordx4 v[176:179], v[180:181], off offset:512 nt
	s_nop 0
	global_load_dwordx4 v[180:183], v[180:181], off offset:576 nt
	s_nop 0
	global_load_dwordx4 v[184:187], v[220:221], off nt
	global_load_dwordx4 v[188:191], v[220:221], off offset:64 nt
	global_load_dwordx4 v[206:209], v[220:221], off offset:512 nt
	s_nop 0
	global_load_dwordx4 v[220:223], v[220:221], off offset:576 nt
	v_lshl_add_u64 v[228:229], s[28:29], 0, v[134:135]
	v_lshl_add_u64 v[226:227], s[28:29], 0, v[226:227]
	v_lshl_add_u64 v[228:229], v[228:229], 0, v[130:131]
	v_lshl_add_u64 v[192:193], s[28:29], 0, v[192:193]
	v_lshl_add_u64 v[224:225], s[28:29], 0, v[224:225]
	v_lshl_add_u64 v[226:227], v[226:227], 0, v[130:131]
	v_lshl_add_u64 v[192:193], v[192:193], 0, v[130:131]
	v_lshl_add_u64 v[224:225], v[224:225], 0, v[130:131]
	s_andn2_b64 vcc, exec, s[4:5]
	s_mov_b64 s[4:5], -1
	s_waitcnt vmcnt(0)
	v_pk_add_f32 v[128:129], v[128:129], v[138:139]
	v_pk_add_f32 v[126:127], v[126:127], v[136:137]
	v_pk_add_f32 v[122:123], v[122:123], v[140:141]
	v_pk_add_f32 v[110:111], v[110:111], v[156:157]
	v_pk_add_f32 v[94:95], v[94:95], v[172:173]
	v_pk_add_f32 v[78:79], v[78:79], v[180:181]
	v_pk_add_f32 v[72:73], v[72:73], v[208:209]
	v_pk_add_f32 v[70:71], v[70:71], v[206:207]
	v_pk_add_f32 v[68:69], v[68:69], v[222:223]
	v_pk_add_f32 v[66:67], v[66:67], v[220:221]
	v_lshl_add_u64 v[136:137], v[134:135], 0, s[42:43]
	v_lshl_add_u64 v[138:139], v[134:135], 0, s[44:45]
	v_lshl_add_u64 v[140:141], v[134:135], 0, s[46:47]
	v_lshl_add_u64 v[134:135], v[134:135], 0, s[48:49]
	v_pk_add_f32 v[124:125], v[124:125], v[142:143]
	v_pk_add_f32 v[116:117], v[116:117], v[146:147]
	v_pk_add_f32 v[114:115], v[114:115], v[144:145]
	v_pk_add_f32 v[108:109], v[108:109], v[150:151]
	v_pk_add_f32 v[106:107], v[106:107], v[148:149]
	v_pk_add_f32 v[120:121], v[120:121], v[154:155]
	v_pk_add_f32 v[118:119], v[118:119], v[152:153]
	v_pk_add_f32 v[112:113], v[112:113], v[158:159]
	v_pk_add_f32 v[100:101], v[100:101], v[162:163]
	v_pk_add_f32 v[98:99], v[98:99], v[160:161]
	v_pk_add_f32 v[92:93], v[92:93], v[166:167]
	v_pk_add_f32 v[90:91], v[90:91], v[164:165]
	v_pk_add_f32 v[104:105], v[104:105], v[170:171]
	v_pk_add_f32 v[102:103], v[102:103], v[168:169]
	v_pk_add_f32 v[96:97], v[96:97], v[174:175]
	v_pk_add_f32 v[84:85], v[84:85], v[178:179]
	v_pk_add_f32 v[82:83], v[82:83], v[176:177]
	v_pk_add_f32 v[80:81], v[80:81], v[182:183]
	v_pk_add_f32 v[88:89], v[88:89], v[186:187]
	v_pk_add_f32 v[86:87], v[86:87], v[184:185]
	v_pk_add_f32 v[76:77], v[76:77], v[190:191]
	v_pk_add_f32 v[74:75], v[74:75], v[188:189]
	global_store_dwordx4 v[228:229], v[126:129], off
	global_store_dwordx4 v[228:229], v[122:125], off offset:64
	global_store_dwordx4 v[228:229], v[114:117], off offset:512
	global_store_dwordx4 v[228:229], v[106:109], off offset:576
	global_store_dwordx4 v[192:193], v[118:121], off
	global_store_dwordx4 v[192:193], v[110:113], off offset:64
	global_store_dwordx4 v[192:193], v[98:101], off offset:512
	global_store_dwordx4 v[192:193], v[90:93], off offset:576
	global_store_dwordx4 v[224:225], v[102:105], off
	global_store_dwordx4 v[224:225], v[94:97], off offset:64
	global_store_dwordx4 v[224:225], v[82:85], off offset:512
	global_store_dwordx4 v[224:225], v[78:81], off offset:576
	global_store_dwordx4 v[226:227], v[86:89], off
	global_store_dwordx4 v[226:227], v[74:77], off offset:64
	global_store_dwordx4 v[226:227], v[70:73], off offset:512
	global_store_dwordx4 v[226:227], v[66:69], off offset:576
	v_lshl_add_u64 v[78:79], v[132:133], 0, v[136:137]
	v_lshl_add_u64 v[94:95], v[132:133], 0, v[138:139]
	v_lshl_add_u64 v[110:111], v[132:133], 0, v[140:141]
	v_lshl_add_u64 v[126:127], v[132:133], 0, v[134:135]
	global_load_dwordx4 v[66:69], v[78:79], off nt
	global_load_dwordx4 v[70:73], v[78:79], off offset:64 nt
	global_load_dwordx4 v[74:77], v[78:79], off offset:512 nt
	s_nop 0
	global_load_dwordx4 v[78:81], v[78:79], off offset:576 nt
	s_nop 0
	global_load_dwordx4 v[82:85], v[94:95], off nt
	global_load_dwordx4 v[86:89], v[94:95], off offset:64 nt
	global_load_dwordx4 v[90:93], v[94:95], off offset:512 nt
	s_nop 0
	global_load_dwordx4 v[94:97], v[94:95], off offset:576 nt
	s_nop 0
	global_load_dwordx4 v[98:101], v[110:111], off nt
	global_load_dwordx4 v[102:105], v[110:111], off offset:64 nt
	global_load_dwordx4 v[106:109], v[110:111], off offset:512 nt
	s_nop 0
	global_load_dwordx4 v[110:113], v[110:111], off offset:576 nt
	s_nop 0
	global_load_dwordx4 v[114:117], v[126:127], off nt
	global_load_dwordx4 v[118:121], v[126:127], off offset:64 nt
	global_load_dwordx4 v[122:125], v[126:127], off offset:512 nt
	s_nop 0
	global_load_dwordx4 v[126:129], v[126:127], off offset:576 nt
	v_lshl_add_u64 v[132:133], s[28:29], 0, v[136:137]
	v_lshl_add_u64 v[136:137], s[28:29], 0, v[138:139]
	v_lshl_add_u64 v[138:139], s[28:29], 0, v[140:141]
	v_lshl_add_u64 v[134:135], s[28:29], 0, v[134:135]
	v_lshl_add_u64 v[132:133], v[132:133], 0, v[130:131]
	v_lshl_add_u64 v[136:137], v[136:137], 0, v[130:131]
	v_lshl_add_u64 v[138:139], v[138:139], 0, v[130:131]
	v_lshl_add_u64 v[130:131], v[134:135], 0, v[130:131]
	s_waitcnt vmcnt(15)
; #define PG8_BAR __builtin_amdgcn_s_barrier()
; template <class Epi, class Sched, bool ALIGN_EPI, bool FP8 = false>
; __device__ __forceinline__ void gemm_phase(LAS unsigned char* lds, const Gemm g, const Sched& S, const Epi& E) {
;     ...
;         if (!has_next) break;
; #pragma unroll
;         for (int a = 0; a < 2; ++a)
; #pragma unroll
;             for (int b = 0; b < 2; ++b)
; #pragma unroll
;                 for (int m = 0; m < 4; ++m)
; #pragma unroll
;                     for (int n = 0; n < 2; ++n) acc[a][b][m][n] = (f32x4){0.f, 0.f, 0.f, 0.f};
;         cur = nxt; cB = nB; ++ui;
;         if constexpr (ALIGN_EPI) { if (wr == 1) PG8_BAR; }
;     __device__ __forceinline__ void operator()(const f32x4 (&acc)[2][2][4][2], const Unit& u, int wr, int wc, int fr, int fq, const LAS float* bl) const {
;     ...
;             for (int m = 0; m < 4; ++m) { const size_t off = (size_t)(row0 + ai * HALF + m * 16) * ldc + col0;
; #pragma unroll
;                 for (int bj = 0; bj < 2; ++bj)
; #pragma unroll
;                     for (int n = 0; n < 2; ++n) *(f32x4*)(out + off + bj * HALF + n * 16) = res[m][bj][n] + acc[ai][bj][m][n]; }
;         }
	v_pk_add_f32 v[56:57], v[56:57], v[68:69]
	v_pk_add_f32 v[54:55], v[54:55], v[66:67]
	s_waitcnt vmcnt(14)
	v_pk_add_f32 v[52:53], v[52:53], v[72:73]
	v_pk_add_f32 v[50:51], v[50:51], v[70:71]
	s_waitcnt vmcnt(13)
	v_pk_add_f32 v[44:45], v[44:45], v[76:77]
	v_pk_add_f32 v[42:43], v[42:43], v[74:75]
	s_waitcnt vmcnt(0)
	v_pk_add_f32 v[4:5], v[4:5], v[128:129]
	v_pk_add_f32 v[2:3], v[2:3], v[126:127]
	v_pk_add_f32 v[36:37], v[36:37], v[80:81]
	v_pk_add_f32 v[34:35], v[34:35], v[78:79]
	v_pk_add_f32 v[48:49], v[48:49], v[84:85]
	v_pk_add_f32 v[46:47], v[46:47], v[82:83]
	v_pk_add_f32 v[40:41], v[40:41], v[88:89]
	v_pk_add_f32 v[38:39], v[38:39], v[86:87]
	v_pk_add_f32 v[28:29], v[28:29], v[92:93]
	v_pk_add_f32 v[26:27], v[26:27], v[90:91]
	v_pk_add_f32 v[12:13], v[12:13], v[96:97]
	v_pk_add_f32 v[10:11], v[10:11], v[94:95]
	v_pk_add_f32 v[32:33], v[32:33], v[100:101]
	v_pk_add_f32 v[30:31], v[30:31], v[98:99]
	v_pk_add_f32 v[20:21], v[20:21], v[104:105]
	v_pk_add_f32 v[18:19], v[18:19], v[102:103]
	v_pk_add_f32 v[64:65], v[64:65], v[108:109]
	v_pk_add_f32 v[62:63], v[62:63], v[106:107]
	v_pk_add_f32 v[60:61], v[60:61], v[112:113]
	v_pk_add_f32 v[58:59], v[58:59], v[110:111]
	v_pk_add_f32 v[16:17], v[16:17], v[116:117]
	v_pk_add_f32 v[14:15], v[14:15], v[114:115]
	v_pk_add_f32 v[8:9], v[8:9], v[120:121]
	v_pk_add_f32 v[6:7], v[6:7], v[118:119]
	v_pk_add_f32 v[24:25], v[24:25], v[124:125]
	v_pk_add_f32 v[22:23], v[22:23], v[122:123]
	global_store_dwordx4 v[132:133], v[54:57], off
	global_store_dwordx4 v[132:133], v[50:53], off offset:64
	global_store_dwordx4 v[132:133], v[42:45], off offset:512
	global_store_dwordx4 v[132:133], v[34:37], off offset:576
	global_store_dwordx4 v[136:137], v[46:49], off
	global_store_dwordx4 v[136:137], v[38:41], off offset:64
	global_store_dwordx4 v[136:137], v[26:29], off offset:512
	global_store_dwordx4 v[136:137], v[10:13], off offset:576
	global_store_dwordx4 v[138:139], v[30:33], off
	global_store_dwordx4 v[138:139], v[18:21], off offset:64
	global_store_dwordx4 v[138:139], v[62:65], off offset:512
	global_store_dwordx4 v[138:139], v[58:61], off offset:576
	global_store_dwordx4 v[130:131], v[14:17], off
	global_store_dwordx4 v[130:131], v[6:9], off offset:64
	global_store_dwordx4 v[130:131], v[22:25], off offset:512
	global_store_dwordx4 v[130:131], v[2:5], off offset:576
	s_cbranch_vccnz .LBB0_1090
.Lp6x_tail:
	s_andn2_b64 vcc, exec, s[16:17]
	s_cbranch_vccnz .LBB0_1089
	s_barrier
	s_branch .LBB0_1089
.Lp6x_epi:
	s_nop 7
	s_waitcnt lgkmcnt(0)
	v_lshl_add_u32 v184, s75, 8, v213
	v_lshl_or_b32 v130, s54, 8, v214
	v_ashrrev_i32_e32 v185, 31, v184
	v_ashrrev_i32_e32 v131, 31, v130
	v_lshlrev_b64 v[134:135], 13, v[184:185]
	v_or_b32_e32 v152, 16, v184
	v_or_b32_e32 v168, 32, v184
	v_or_b32_e32 v184, 48, v184
	v_lshlrev_b64 v[130:131], 2, v[130:131]
	v_ashrrev_i32_e32 v153, 31, v152
	v_ashrrev_i32_e32 v169, 31, v168
	v_ashrrev_i32_e32 v185, 31, v184
	v_lshlrev_b64 v[192:193], 13, v[152:153]
	v_lshlrev_b64 v[224:225], 13, v[168:169]
	v_lshlrev_b64 v[226:227], 13, v[184:185]
	v_lshl_add_u64 v[228:229], s[28:29], 0, v[134:135]
	v_lshl_add_u64 v[226:227], s[28:29], 0, v[226:227]
	v_lshl_add_u64 v[228:229], v[228:229], 0, v[130:131]
	v_lshl_add_u64 v[192:193], s[28:29], 0, v[192:193]
	v_lshl_add_u64 v[224:225], s[28:29], 0, v[224:225]
	v_lshl_add_u64 v[226:227], v[226:227], 0, v[130:131]
	v_lshl_add_u64 v[192:193], v[192:193], 0, v[130:131]
	v_lshl_add_u64 v[224:225], v[224:225], 0, v[130:131]
	s_andn2_b64 vcc, exec, s[4:5]
	s_mov_b64 s[4:5], -1
	global_store_dwordx4 v[228:229], v[126:129], off
	global_store_dwordx4 v[228:229], v[122:125], off offset:64
	global_store_dwordx4 v[228:229], v[114:117], off offset:512
	global_store_dwordx4 v[228:229], v[106:109], off offset:576
	global_store_dwordx4 v[192:193], v[118:121], off
	global_store_dwordx4 v[192:193], v[110:113], off offset:64
	global_store_dwordx4 v[192:193], v[98:101], off offset:512
	global_store_dwordx4 v[192:193], v[90:93], off offset:576
	global_store_dwordx4 v[224:225], v[102:105], off
	global_store_dwordx4 v[224:225], v[94:97], off offset:64
	global_store_dwordx4 v[224:225], v[82:85], off offset:512
	global_store_dwordx4 v[224:225], v[78:81], off offset:576
	global_store_dwordx4 v[226:227], v[86:89], off
	global_store_dwordx4 v[226:227], v[74:77], off offset:64
	global_store_dwordx4 v[226:227], v[70:73], off offset:512
	global_store_dwordx4 v[226:227], v[66:69], off offset:576
	v_lshl_add_u64 v[136:137], v[134:135], 0, s[42:43]
	v_lshl_add_u64 v[138:139], v[134:135], 0, s[44:45]
	v_lshl_add_u64 v[140:141], v[134:135], 0, s[46:47]
	v_lshl_add_u64 v[134:135], v[134:135], 0, s[48:49]
	v_lshl_add_u64 v[132:133], s[28:29], 0, v[136:137]
	v_lshl_add_u64 v[136:137], s[28:29], 0, v[138:139]
	v_lshl_add_u64 v[138:139], s[28:29], 0, v[140:141]
	v_lshl_add_u64 v[134:135], s[28:29], 0, v[134:135]
	v_lshl_add_u64 v[132:133], v[132:133], 0, v[130:131]
	v_lshl_add_u64 v[136:137], v[136:137], 0, v[130:131]
	v_lshl_add_u64 v[138:139], v[138:139], 0, v[130:131]
	v_lshl_add_u64 v[130:131], v[134:135], 0, v[130:131]
	global_store_dwordx4 v[132:133], v[54:57], off
	global_store_dwordx4 v[132:133], v[50:53], off offset:64
	global_store_dwordx4 v[132:133], v[42:45], off offset:512
	global_store_dwordx4 v[132:133], v[34:37], off offset:576
	global_store_dwordx4 v[136:137], v[46:49], off
	global_store_dwordx4 v[136:137], v[38:41], off offset:64
	global_store_dwordx4 v[136:137], v[26:29], off offset:512
	global_store_dwordx4 v[136:137], v[10:13], off offset:576
	global_store_dwordx4 v[138:139], v[30:33], off
	global_store_dwordx4 v[138:139], v[18:21], off offset:64
	global_store_dwordx4 v[138:139], v[62:65], off offset:512
	global_store_dwordx4 v[138:139], v[58:61], off offset:576
	global_store_dwordx4 v[130:131], v[14:17], off
	global_store_dwordx4 v[130:131], v[6:9], off offset:64
	global_store_dwordx4 v[130:131], v[22:25], off offset:512
	global_store_dwordx4 v[130:131], v[2:5], off offset:576
	s_cbranch_vccnz .LBB0_1090
	s_branch .Lp6x_tail
